# code placement: five dead 4-byte pads restore the baseline's mod-8 byte phase of every GEMM loop that earlier edits had shifted by 4 (P4, P6, P7, P9-entry, P15)
# speedup vs baseline: 1.0052x; 1.0052x over previous
;     __device__ __forceinline__ const char* Bptr(const Unit& u) const { return (u.g ? Bkv : Bq) + (size_t)u.pn * BM * ldb * 2; }
; #define PG8_STAGE(bufoff, gbase, voff) do { _Pragma("unroll") for (int _i = 0; _i < 2; ++_i) { unsigned vo_ = (voff)[_i]; asm volatile("" : "+v"(vo_));   \
;         __builtin_amdgcn_global_load_lds((const unsigned*)((const char*)(gbase) + vo_), (LAS unsigned*)(lds + (bufoff) + ldsw + _i * 8192), 16, 0, 0); } } while (0)
; #define PG8_WAIT_V(n) asm volatile("s_waitcnt vmcnt(" #n ")" ::: "memory")
; #define PG8_BAR __builtin_amdgcn_s_barrier()
; #define PG8_AOFFS(dst, un) do { _Pragma("unroll") for (int _h = 0; _h < 2; ++_h) _Pragma("unroll") for (int _i = 0; _i < 2; ++_i) dst[_h][_i] = S.Aoff(un, _h * HALF + Rr[_i]) + (unsigned)Cc[_i] * 2u; } while (0)
;     static __device__ __forceinline__ f32x4 ldb(const bf16_t* p) { return ld4_bf(p); }
;     ...
;     for (int i = 0; i < 2; ++i) { stage_rc(tid * 16 + i * 8192, Rr[i], Cc[i]); const int Rb = Epi::PERM ? ((Rr[i] & ~31) + perm32(Rr[i] & 31)) : Rr[i];
;         voffB[i] = (unsigned)(Rb * S.ldb + Cc[i]) * 2u; }
;     const size_t kstep = (size_t)(BK * 2);
;     const size_t hstepB = (size_t)HALF * S.ldb * 2;
;     const unsigned ldsw = (unsigned)wid * 1024u;
;     const int aoff = lds_byte(wr * 64 + fr, fq * 8), boff = lds_byte(wc * 32 + fr, fq * 8);
;     ...
;     PG8_AOFFS(va, cur);
;     const char* cB = S.Bptr(cur);
;     PG8_STAGE(PG8_SB(0, 0), cB, voffB); PG8_STAGE(PG8_SB(0, 1), cB + hstepB, voffB); PG8_STAGE(PG8_SA(0, 0), Abase, va[0]); PG8_STAGE(PG8_SA(0, 1), Abase, va[1]);
;     if (wr == 1) PG8_BAR;
;     PG8_WAIT_V(2); PG8_BAR;
;     PG8_STAGE(PG8_SB(1, 0), cB + kstep, voffB); PG8_STAGE(PG8_SA(1, 0), Abase + kstep, va[0]); PG8_STAGE(PG8_SB(1, 1), cB + hstepB + kstep, voffB);
;     PG8_WAIT_V(6); PG8_BAR;
.LBB0_1189:
	s_add_u32 s51, s36, 0x1c2c0000
	s_addc_u32 s53, s37, 0
	s_add_u32 s54, s36, 0x104000
	s_addc_u32 s55, s37, 0
	s_lshl_b32 s14, s14, 5
	v_mov_b32_e32 v166, v187
	v_mov_b32_e32 v167, 0
	s_and_b32 s23, s14, 0x60
	s_waitcnt vmcnt(2)
	s_barrier
	s_mov_b64 s[14:15], 0x80
	v_lshl_add_u64 v[2:3], s[28:29], 0, v[166:167]
	s_add_i32 m0, s43, 0x18000
	v_lshl_add_u64 v[2:3], v[2:3], 0, s[14:15]
	v_mov_b32_e32 v166, v189
	s_lshl_b32 s22, s19, 13
	global_load_lds_dwordx4 v[2:3], off
	s_add_i32 m0, s43, 0x1a000
	v_lshl_add_u64 v[2:3], s[28:29], 0, v[166:167]
	v_lshl_add_u64 v[2:3], v[2:3], 0, s[14:15]
	s_add_u32 s16, s36, 0x28ec0080
	global_load_lds_dwordx4 v[2:3], off
	s_addc_u32 s17, s37, 0
	v_mov_b32_e32 v2, v194
	s_add_i32 s56, s43, 0x8000
	s_mov_b32 m0, s56
	s_add_i32 s57, s43, 0xa000
	global_load_lds_dwordx4 v2, s[16:17]
	v_mov_b32_e32 v2, v195
	s_mov_b32 m0, s57
	s_add_u32 s20, s28, 0x80080
	global_load_lds_dwordx4 v2, s[16:17]
	v_mov_b32_e32 v2, v187
	s_addc_u32 s21, s29, 0
	s_add_i32 m0, s43, 0x1c000
	v_lshlrev_b32_e32 v4, 2, v191
	global_load_lds_dwordx4 v2, s[20:21]
	v_mov_b32_e32 v2, v189
	s_add_i32 m0, s43, 0x1e000
	v_lshl_or_b32 v3, v191, 6, v192
	global_load_lds_dwordx4 v2, s[20:21]
	v_lshl_or_b32 v2, s19, 6, v191
	v_or_b32_e32 v166, 16, v2
	v_lshlrev_b64 v[170:171], 11, v[166:167]
	v_or_b32_e32 v166, 32, v2
	v_lshlrev_b64 v[172:173], 11, v[166:167]
	v_or_b32_e32 v166, 48, v2
	v_lshlrev_b64 v[174:175], 11, v[166:167]
	v_add_u32_e32 v166, 0x80, v2
	v_and_b32_e32 v4, 32, v4
	v_lshlrev_b64 v[176:177], 11, v[166:167]
	v_add_u32_e32 v166, 0x90, v2
	v_bitop3_b32 v4, v3, s22, v4 bitop3:0xde
	v_lshl_or_b32 v198, s23, 7, v193
	s_waitcnt vmcnt(6)
	v_mov_b32_e32 v3, v167
	v_lshlrev_b64 v[178:179], 11, v[166:167]
	v_add_u32_e32 v166, 0xa0, v2
	s_cmpk_lt_u32 s18, 0x100
	v_lshlrev_b64 v[168:169], 11, v[2:3]
	v_lshlrev_b64 v[180:181], 11, v[166:167]
	v_add_u32_e32 v166, 0xb0, v2
	v_add_u32_e32 v2, 0, v198
	s_sext_i32_i8 s61, s6
	s_cselect_b64 s[18:19], -1, 0
	v_lshlrev_b64 v[182:183], 11, v[166:167]
	v_lshl_or_b32 v199, v190, 2, s23
	v_add_u32_e32 v200, 0x10000, v2
	v_add_u32_e32 v201, 0x14000, v2
	v_add_u32_e32 v202, 0, v4
	s_mov_b32 s58, 0
	s_barrier
	s_branch .LBB0_1192
	s_nop 0

;     __device__ __forceinline__ const char* Bptr(const Unit& u) const { return (u.g ? Bkv : Bq) + (size_t)u.pn * BM * ldb * 2; }
; #define PG8_STAGE(bufoff, gbase, voff) do { _Pragma("unroll") for (int _i = 0; _i < 2; ++_i) { unsigned vo_ = (voff)[_i]; asm volatile("" : "+v"(vo_));   \
;         __builtin_amdgcn_global_load_lds((const unsigned*)((const char*)(gbase) + vo_), (LAS unsigned*)(lds + (bufoff) + ldsw + _i * 8192), 16, 0, 0); } } while (0)
; #define PG8_WAIT_V(n) asm volatile("s_waitcnt vmcnt(" #n ")" ::: "memory")
; #define PG8_BAR __builtin_amdgcn_s_barrier()
; #define PG8_AOFFS(dst, un) do { _Pragma("unroll") for (int _h = 0; _h < 2; ++_h) _Pragma("unroll") for (int _i = 0; _i < 2; ++_i) dst[_h][_i] = S.Aoff(un, _h * HALF + Rr[_i]) + (unsigned)Cc[_i] * 2u; } while (0)
;     static __device__ __forceinline__ f32x4 ldb(const bf16_t* p) { return ld4_bf(p); }
;     ...
;     for (int i = 0; i < 2; ++i) { stage_rc(tid * 16 + i * 8192, Rr[i], Cc[i]); const int Rb = Epi::PERM ? ((Rr[i] & ~31) + perm32(Rr[i] & 31)) : Rr[i];
;         voffB[i] = (unsigned)(Rb * S.ldb + Cc[i]) * 2u; }
;     const size_t kstep = (size_t)(BK * 2);
;     const size_t hstepB = (size_t)HALF * S.ldb * 2;
;     const unsigned ldsw = (unsigned)wid * 1024u;
;     const int aoff = lds_byte(wr * 64 + fr, fq * 8), boff = lds_byte(wc * 32 + fr, fq * 8);
;     ...
;     PG8_AOFFS(va, cur);
;     const char* cB = S.Bptr(cur);
;     PG8_STAGE(PG8_SB(0, 0), cB, voffB); PG8_STAGE(PG8_SB(0, 1), cB + hstepB, voffB); PG8_STAGE(PG8_SA(0, 0), Abase, va[0]); PG8_STAGE(PG8_SA(0, 1), Abase, va[1]);
;     if (wr == 1) PG8_BAR;
;     PG8_WAIT_V(2); PG8_BAR;
;     PG8_STAGE(PG8_SB(1, 0), cB + kstep, voffB); PG8_STAGE(PG8_SA(1, 0), Abase + kstep, va[0]); PG8_STAGE(PG8_SB(1, 1), cB + hstepB + kstep, voffB);
;     PG8_WAIT_V(6); PG8_BAR;
.LBB0_1519:
	s_add_u32 s53, s36, 0x1c2c0000
	s_addc_u32 s54, s37, 0
	s_add_u32 s55, s36, 0x202c0000
	s_addc_u32 s56, s37, 0
	s_add_u32 s57, s36, 0x10a000
	s_addc_u32 s58, s37, 0
	s_lshl_b32 s16, s16, 5
	v_mov_b32_e32 v194, v215
	v_mov_b32_e32 v195, 0
	s_and_b32 s24, s16, 0x60
	s_waitcnt vmcnt(2)
	s_barrier
	s_mov_b64 s[16:17], 0x80
	v_lshl_add_u64 v[2:3], s[30:31], 0, v[194:195]
	s_add_i32 m0, s45, 0x18000
	v_lshl_add_u64 v[2:3], v[2:3], 0, s[16:17]
	v_mov_b32_e32 v194, v217
	s_lshl_b32 s22, s2, 13
	global_load_lds_dwordx4 v[2:3], off
	s_add_i32 m0, s45, 0x1a000
	v_lshl_add_u64 v[2:3], s[30:31], 0, v[194:195]
	v_lshl_add_u64 v[2:3], v[2:3], 0, s[16:17]
	s_add_u32 s18, s36, 0x2d2c0080
	global_load_lds_dwordx4 v[2:3], off
	s_addc_u32 s19, s37, 0
	v_mov_b32_e32 v2, v222
	s_add_i32 s59, s45, 0x8000
	s_mov_b32 m0, s59
	s_add_i32 s60, s45, 0xa000
	global_load_lds_dwordx4 v2, s[18:19]
	v_mov_b32_e32 v2, v223
	s_mov_b32 m0, s60
	s_add_u32 s20, s30, 0xb0080
	global_load_lds_dwordx4 v2, s[18:19]
	v_mov_b32_e32 v2, v215
	s_addc_u32 s21, s31, 0
	s_add_i32 m0, s45, 0x1c000
	v_lshlrev_b32_e32 v4, 2, v219
	global_load_lds_dwordx4 v2, s[20:21]
	v_mov_b32_e32 v2, v217
	s_add_i32 m0, s45, 0x1e000
	v_lshl_or_b32 v3, v219, 6, v220
	global_load_lds_dwordx4 v2, s[20:21]
	v_lshl_or_b32 v2, s2, 6, v219
	v_or_b32_e32 v194, 16, v2
	v_lshlrev_b64 v[198:199], 11, v[194:195]
	v_or_b32_e32 v194, 32, v2
	v_lshlrev_b64 v[200:201], 11, v[194:195]
	v_or_b32_e32 v194, 48, v2
	v_lshlrev_b64 v[202:203], 11, v[194:195]
	v_add_u32_e32 v194, 0x80, v2
	v_and_b32_e32 v4, 32, v4
	v_lshlrev_b64 v[204:205], 11, v[194:195]
	v_add_u32_e32 v194, 0x90, v2
	v_bitop3_b32 v4, v3, s22, v4 bitop3:0xde
	v_lshl_or_b32 v226, s24, 7, v221
	s_waitcnt vmcnt(6)
	v_mov_b32_e32 v3, v195
	v_lshlrev_b64 v[206:207], 11, v[194:195]
	v_add_u32_e32 v194, 0xa0, v2
	s_cmpk_lt_u32 s14, 0x100
	v_lshlrev_b64 v[196:197], 11, v[2:3]
	v_lshlrev_b64 v[208:209], 11, v[194:195]
	v_add_u32_e32 v194, 0xb0, v2
	v_add_u32_e32 v2, 0, v226
	s_sext_i32_i8 s66, s3
	s_cselect_b64 s[20:21], -1, 0
	v_lshlrev_b64 v[210:211], 11, v[194:195]
	v_lshl_or_b32 v227, v218, 2, s24
	v_add_u32_e32 v228, 0x10000, v2
	v_add_u32_e32 v229, 0x14000, v2
	v_add_u32_e32 v230, 0, v4
	v_mov_b32_e32 v231, 0x7f
	s_mov_b32 s22, 0x3b000000
	s_add_i32 s61, s45, 0xc000
	s_mov_b32 s62, 0
	s_barrier
	s_branch .LBB0_1522
	s_nop 0

;     __device__ __forceinline__ const char* Bptr(const Unit& u) const { return (u.g ? Bkv : Bq) + (size_t)u.pn * BM * ldb * 2; }
; #define PG8_STAGE(bufoff, gbase, voff) do { _Pragma("unroll") for (int _i = 0; _i < 2; ++_i) { unsigned vo_ = (voff)[_i]; asm volatile("" : "+v"(vo_));   \
;         __builtin_amdgcn_global_load_lds((const unsigned*)((const char*)(gbase) + vo_), (LAS unsigned*)(lds + (bufoff) + ldsw + _i * 8192), 16, 0, 0); } } while (0)
; #define PG8_WAIT_V(n) asm volatile("s_waitcnt vmcnt(" #n ")" ::: "memory")
; #define PG8_BAR __builtin_amdgcn_s_barrier()
; #define PG8_AOFFS(dst, un) do { _Pragma("unroll") for (int _h = 0; _h < 2; ++_h) _Pragma("unroll") for (int _i = 0; _i < 2; ++_i) dst[_h][_i] = S.Aoff(un, _h * HALF + Rr[_i]) + (unsigned)Cc[_i] * 2u; } while (0)
;     static __device__ __forceinline__ f32x4 ldb(const bf16_t* p) { return ld4_bf(p); }
;     ...
;     for (int i = 0; i < 2; ++i) { stage_rc(tid * 16 + i * 8192, Rr[i], Cc[i]); const int Rb = Epi::PERM ? ((Rr[i] & ~31) + perm32(Rr[i] & 31)) : Rr[i];
;         voffB[i] = (unsigned)(Rb * S.ldb + Cc[i]) * 2u; }
;     const size_t kstep = (size_t)(BK * 2);
;     const size_t hstepB = (size_t)HALF * S.ldb * 2;
;     const unsigned ldsw = (unsigned)wid * 1024u;
;     const int aoff = lds_byte(wr * 64 + fr, fq * 8), boff = lds_byte(wc * 32 + fr, fq * 8);
;     ...
;     PG8_AOFFS(va, cur);
;     const char* cB = S.Bptr(cur);
;     PG8_STAGE(PG8_SB(0, 0), cB, voffB); PG8_STAGE(PG8_SB(0, 1), cB + hstepB, voffB); PG8_STAGE(PG8_SA(0, 0), Abase, va[0]); PG8_STAGE(PG8_SA(0, 1), Abase, va[1]);
;     if (wr == 1) PG8_BAR;
;     PG8_WAIT_V(2); PG8_BAR;
;     PG8_STAGE(PG8_SB(1, 0), cB + kstep, voffB); PG8_STAGE(PG8_SA(1, 0), Abase + kstep, va[0]); PG8_STAGE(PG8_SB(1, 1), cB + hstepB + kstep, voffB);
;     PG8_WAIT_V(6); PG8_BAR;
.LBB0_1552:
	v_mov_b32_e32 v194, v215
	v_mov_b32_e32 v195, 0
	s_add_u32 s60, s36, 0x5aec0000
	s_waitcnt vmcnt(2)
	s_barrier
	s_mov_b64 s[14:15], 0x80
	v_lshl_add_u64 v[2:3], s[42:43], 0, v[194:195]
	s_addc_u32 s61, s37, 0
	s_lshl_b32 s3, s3, 5
	s_add_i32 m0, s51, 0x18000
	v_lshl_add_u64 v[2:3], v[2:3], 0, s[14:15]
	v_mov_b32_e32 v194, v217
	s_lshl_b32 s19, s2, 13
	s_and_b32 s3, s3, 0x60
	global_load_lds_dwordx4 v[2:3], off
	s_add_i32 m0, s51, 0x1a000
	v_lshl_add_u64 v[2:3], s[42:43], 0, v[194:195]
	v_lshl_add_u64 v[2:3], v[2:3], 0, s[14:15]
	s_add_u32 s16, s36, 0x2d2c0080
	global_load_lds_dwordx4 v[2:3], off
	s_addc_u32 s17, s37, 0
	v_mov_b32_e32 v2, v222
	s_add_i32 s62, s51, 0x8000
	s_mov_b32 m0, s62
	s_add_i32 s63, s51, 0xa000
	global_load_lds_dwordx4 v2, s[16:17]
	v_mov_b32_e32 v2, v223
	s_mov_b32 m0, s63
	s_add_u32 s20, s42, 0xb0080
	global_load_lds_dwordx4 v2, s[16:17]
	v_mov_b32_e32 v2, v215
	s_addc_u32 s21, s43, 0
	s_add_i32 m0, s51, 0x1c000
	v_lshlrev_b32_e32 v4, 2, v219
	global_load_lds_dwordx4 v2, s[20:21]
	v_mov_b32_e32 v2, v217
	s_add_i32 m0, s51, 0x1e000
	v_lshl_or_b32 v3, v219, 6, v220
	global_load_lds_dwordx4 v2, s[20:21]
	v_lshl_or_b32 v2, s2, 6, v219
	v_or_b32_e32 v194, 16, v2
	v_lshlrev_b64 v[198:199], 13, v[194:195]
	v_or_b32_e32 v194, 32, v2
	v_lshlrev_b64 v[200:201], 13, v[194:195]
	v_or_b32_e32 v194, 48, v2
	v_lshlrev_b64 v[202:203], 13, v[194:195]
	v_add_u32_e32 v194, 0x80, v2
	v_and_b32_e32 v4, 32, v4
	v_lshlrev_b64 v[204:205], 13, v[194:195]
	v_add_u32_e32 v194, 0x90, v2
	v_bitop3_b32 v4, v3, s19, v4 bitop3:0xde
	v_lshl_or_b32 v219, s3, 7, v221
	s_waitcnt vmcnt(6)
	s_cmpk_lt_u32 s18, 0x100
	v_mov_b32_e32 v3, v195
	v_lshlrev_b64 v[206:207], 13, v[194:195]
	v_add_u32_e32 v194, 0xa0, v2
	s_cselect_b64 s[18:19], -1, 0
	v_lshlrev_b64 v[196:197], 13, v[2:3]
	v_lshlrev_b64 v[208:209], 13, v[194:195]
	v_add_u32_e32 v194, 0xb0, v2
	s_add_u32 s20, s36, 0x13a000
	v_add_u32_e32 v2, 0, v219
	s_brev_b32 s24, 31
	v_lshlrev_b64 v[210:211], 13, v[194:195]
	s_addc_u32 s21, s37, 0
	v_lshl_or_b32 v218, v218, 2, s3
	v_add_u32_e32 v220, 0x10000, v2
	v_add_u32_e32 v221, 0x14000, v2
	v_add_u32_e32 v226, 0, v4
	v_mov_b32_e32 v227, 0x7f
	s_mov_b32 s22, 0x3b000000
	s_mov_b32 s25, -1
	s_barrier
	s_branch .LBB0_1555
	s_nop 0

;     __device__ __forceinline__ const char* Bptr(const Unit& u) const { return (u.g ? Bkv : Bq) + (size_t)u.pn * BM * ldb * 2; }
; #define PG8_STAGE(bufoff, gbase, voff) do { _Pragma("unroll") for (int _i = 0; _i < 2; ++_i) { unsigned vo_ = (voff)[_i]; asm volatile("" : "+v"(vo_));   \
;         __builtin_amdgcn_global_load_lds((const unsigned*)((const char*)(gbase) + vo_), (LAS unsigned*)(lds + (bufoff) + ldsw + _i * 8192), 16, 0, 0); } } while (0)
; #define PG8_WAIT_V(n) asm volatile("s_waitcnt vmcnt(" #n ")" ::: "memory")
; #define PG8_BAR __builtin_amdgcn_s_barrier()
; #define PG8_AOFFS(dst, un) do { _Pragma("unroll") for (int _h = 0; _h < 2; ++_h) _Pragma("unroll") for (int _i = 0; _i < 2; ++_i) dst[_h][_i] = S.Aoff(un, _h * HALF + Rr[_i]) + (unsigned)Cc[_i] * 2u; } while (0)
;     static __device__ __forceinline__ f32x4 ldb(const bf16_t* p) { return ld4_bf(p); }
;     ...
;     for (int i = 0; i < 2; ++i) { stage_rc(tid * 16 + i * 8192, Rr[i], Cc[i]); const int Rb = Epi::PERM ? ((Rr[i] & ~31) + perm32(Rr[i] & 31)) : Rr[i];
;         voffB[i] = (unsigned)(Rb * S.ldb + Cc[i]) * 2u; }
;     const size_t kstep = (size_t)(BK * 2);
;     const size_t hstepB = (size_t)HALF * S.ldb * 2;
;     const unsigned ldsw = (unsigned)wid * 1024u;
;     const int aoff = lds_byte(wr * 64 + fr, fq * 8), boff = lds_byte(wc * 32 + fr, fq * 8);
;     ...
;     PG8_AOFFS(va, cur);
;     const char* cB = S.Bptr(cur);
;     PG8_STAGE(PG8_SB(0, 0), cB, voffB); PG8_STAGE(PG8_SB(0, 1), cB + hstepB, voffB); PG8_STAGE(PG8_SA(0, 0), Abase, va[0]); PG8_STAGE(PG8_SA(0, 1), Abase, va[1]);
;     if (wr == 1) PG8_BAR;
;     PG8_WAIT_V(2); PG8_BAR;
;     PG8_STAGE(PG8_SB(1, 0), cB + kstep, voffB); PG8_STAGE(PG8_SA(1, 0), Abase + kstep, va[0]); PG8_STAGE(PG8_SB(1, 1), cB + hstepB + kstep, voffB);
;     PG8_WAIT_V(6); PG8_BAR;
.LBB0_1743:
	s_add_u32 s18, s36, 0x40000
	s_addc_u32 s19, s37, 0
	s_add_u32 s20, s36, 0x50000
	s_addc_u32 s21, s37, 0
	s_add_u32 s22, s36, 0x180000
	s_addc_u32 s23, s37, 0
	v_mov_b32_e32 v162, v172
	v_mov_b32_e32 v163, 0
	s_add_u32 s24, s36, 0x300000
	s_waitcnt vmcnt(2)
	s_barrier
	s_mov_b64 s[26:27], 0x80
	v_lshl_add_u64 v[2:3], s[62:63], 0, v[162:163]
	s_addc_u32 s25, s37, 0
	s_and_b32 s7, s3, 3
	s_add_i32 m0, s61, 0x18000
	v_lshl_add_u64 v[2:3], v[2:3], 0, s[26:27]
	v_mov_b32_e32 v162, v174
	s_lshl_b32 s3, s2, 13
	s_lshl_b32 s38, s7, 5
	s_lshl_b32 s30, s7, 12
	global_load_lds_dwordx4 v[2:3], off
	s_add_i32 m0, s61, 0x1a000
	v_lshl_add_u64 v[2:3], s[62:63], 0, v[162:163]
	v_lshl_add_u64 v[2:3], v[2:3], 0, s[26:27]
	s_add_u32 s28, s36, 0x24ac0080
	global_load_lds_dwordx4 v[2:3], off
	s_addc_u32 s29, s37, 0
	v_mov_b32_e32 v2, v175
	s_add_i32 s78, s61, 0x8000
	s_mov_b32 m0, s78
	s_add_i32 s79, s61, 0xa000
	global_load_lds_dwordx4 v2, s[28:29]
	v_mov_b32_e32 v2, v176
	s_mov_b32 m0, s79
	s_add_u32 s4, s62, 0x40080
	global_load_lds_dwordx4 v2, s[28:29]
	v_mov_b32_e32 v2, v172
	s_addc_u32 s5, s63, 0
	s_add_i32 m0, s61, 0x1c000
	v_bfe_u32 v3, v0, 4, 2
	global_load_lds_dwordx4 v2, s[4:5]
	v_mov_b32_e32 v2, v174
	s_add_i32 m0, s61, 0x1e000
	v_lshlrev_b32_e32 v4, 4, v3
	global_load_lds_dwordx4 v2, s[4:5]
	v_and_b32_e32 v2, 15, v0
	v_lshlrev_b32_e32 v5, 2, v0
	v_lshl_or_b32 v179, s2, 6, v2
	v_lshl_or_b32 v2, v2, 6, v4
	v_and_b32_e32 v5, 32, v5
	v_lshlrev_b32_e32 v180, 3, v3
	v_bitop3_b32 v6, v2, s3, v5 bitop3:0xde
	v_lshlrev_b32_e32 v2, 6, v0
	s_movk_i32 s2, 0x3c0
	v_and_or_b32 v2, v2, s2, v4
	s_cmpk_lt_u32 s6, 0x100
	v_or_b32_e32 v182, s38, v180
	v_bitop3_b32 v181, s30, v2, v5 bitop3:0xf6
	s_cselect_b64 s[30:31], -1, 0
	v_cmp_eq_u32_e64 s[2:3], 0, v3
	s_cmp_lt_u32 s7, 2
	v_lshlrev_b32_e32 v162, 2, v3
	v_lshlrev_b32_e32 v2, 2, v182
	v_mov_b32_e32 v3, v163
	s_cselect_b64 s[34:35], -1, 0
	s_cmp_eq_u32 s7, 0
	v_lshl_add_u64 v[2:3], s[36:37], 0, v[2:3]
	s_mov_b64 s[6:7], 0x6e000
	s_cselect_b64 s[4:5], -1, 0
	v_lshl_add_u64 v[164:165], v[2:3], 0, s[6:7]
	s_add_u32 s6, s36, s38
	s_addc_u32 s7, s37, 0
	v_lshl_add_u64 v[2:3], s[6:7], 0, v[162:163]
	s_mov_b64 s[6:7], 0x363c0000
	s_waitcnt vmcnt(6)
	v_lshl_add_u64 v[166:167], v[2:3], 0, s[6:7]
	v_add_u32_e32 v2, 0, v181
	v_add_u32_e32 v183, 0x10000, v2
	v_add_u32_e32 v184, 0x14000, v2
	v_mbcnt_lo_u32_b32 v2, -1, 0
	s_movk_i32 s80, 0x100
	v_add_u32_e32 v185, 0, v6
	s_mov_b32 s38, 0x3c010204
	s_movk_i32 s81, 0x7e0
	s_movk_i32 s82, 0xff
	s_mov_b32 s83, 0xc3e00000
	s_movk_i32 s84, 0x600
	s_movk_i32 s88, 0x3f6f
	s_movk_i32 s89, 0x3f5f
	s_movk_i32 s90, 0x3f4f
	s_mov_b32 s91, 0x2d2c0000
	s_mov_b32 s92, 0x20000
	s_mov_b64 s[40:41], 0x4000
	s_mov_b64 s[42:43], 0x8000
	s_mov_b64 s[44:45], 0xc000
	s_mov_b64 s[46:47], 0x20000
	s_mov_b64 s[48:49], 0x24000
	s_mov_b32 s93, 0x24000
	s_mov_b64 s[50:51], 0x28000
	s_mov_b32 s94, 0x28000
	s_mov_b64 s[52:53], 0x2c000
	s_mov_b32 s95, 0x2c000
	v_mbcnt_hi_u32_b32 v186, -1, v2
	v_mov_b32_e32 v187, 0x43e00000
	s_barrier
	s_branch .LBB0_1746
	s_nop 0

;     __device__ __forceinline__ const char* Bptr(const Unit& u) const { return (u.g ? Bkv : Bq) + (size_t)u.pn * BM * ldb * 2; }
; #define PG8_STAGE(bufoff, gbase, voff) do { _Pragma("unroll") for (int _i = 0; _i < 2; ++_i) { unsigned vo_ = (voff)[_i]; asm volatile("" : "+v"(vo_));   \
;         __builtin_amdgcn_global_load_lds((const unsigned*)((const char*)(gbase) + vo_), (LAS unsigned*)(lds + (bufoff) + ldsw + _i * 8192), 16, 0, 0); } } while (0)
; #define PG8_WAIT_V(n) asm volatile("s_waitcnt vmcnt(" #n ")" ::: "memory")
; #define PG8_BAR __builtin_amdgcn_s_barrier()
; #define PG8_AOFFS(dst, un) do { _Pragma("unroll") for (int _h = 0; _h < 2; ++_h) _Pragma("unroll") for (int _i = 0; _i < 2; ++_i) dst[_h][_i] = S.Aoff(un, _h * HALF + Rr[_i]) + (unsigned)Cc[_i] * 2u; } while (0)
;     static __device__ __forceinline__ f32x4 ldb(const bf16_t* p) { return ld4_bf(p); }
;     ...
;     for (int i = 0; i < 2; ++i) { stage_rc(tid * 16 + i * 8192, Rr[i], Cc[i]); const int Rb = Epi::PERM ? ((Rr[i] & ~31) + perm32(Rr[i] & 31)) : Rr[i];
;         voffB[i] = (unsigned)(Rb * S.ldb + Cc[i]) * 2u; }
;     const size_t kstep = (size_t)(BK * 2);
;     const size_t hstepB = (size_t)HALF * S.ldb * 2;
;     const unsigned ldsw = (unsigned)wid * 1024u;
;     const int aoff = lds_byte(wr * 64 + fr, fq * 8), boff = lds_byte(wc * 32 + fr, fq * 8);
;     ...
;     PG8_AOFFS(va, cur);
;     const char* cB = S.Bptr(cur);
;     PG8_STAGE(PG8_SB(0, 0), cB, voffB); PG8_STAGE(PG8_SB(0, 1), cB + hstepB, voffB); PG8_STAGE(PG8_SA(0, 0), Abase, va[0]); PG8_STAGE(PG8_SA(0, 1), Abase, va[1]);
;     if (wr == 1) PG8_BAR;
;     PG8_WAIT_V(2); PG8_BAR;
;     PG8_STAGE(PG8_SB(1, 0), cB + kstep, voffB); PG8_STAGE(PG8_SA(1, 0), Abase + kstep, va[0]); PG8_STAGE(PG8_SB(1, 1), cB + hstepB + kstep, voffB);
;     PG8_WAIT_V(6); PG8_BAR;
.LBB0_2626:
	s_add_u32 s20, s36, 0x24ac0000
	v_mov_b32_e32 v194, v203
	s_addc_u32 s21, s37, 0
	s_lshl_b32 s3, s3, 5
	s_waitcnt vmcnt(2)
	s_barrier
	s_mov_b64 s[22:23], 0x80
	v_lshl_add_u64 v[6:7], v[2:3], 0, v[194:195]
	s_and_b32 s3, s3, 0x60
	s_add_i32 m0, s60, 0x18000
	v_lshl_add_u64 v[6:7], v[6:7], 0, s[22:23]
	s_lshl_b32 s5, s2, 13
	s_lshl_b32 s28, s3, 7
	global_load_lds_dwordx4 v[6:7], off
	v_mov_b32_e32 v194, v205
	s_add_i32 m0, s60, 0x1a000
	s_add_u32 s24, s36, 0x2d2c0080
	v_lshl_add_u64 v[6:7], v[2:3], 0, v[194:195]
	v_lshl_add_u64 v[6:7], v[6:7], 0, s[22:23]
	s_addc_u32 s25, s37, 0
	v_mov_b32_e32 v5, v206
	s_add_i32 s70, s60, 0x8000
	global_load_lds_dwordx4 v[6:7], off
	s_mov_b32 m0, s70
	s_add_i32 s71, s60, 0xa000
	global_load_lds_dwordx4 v5, s[24:25]
	v_mov_b32_e32 v5, v207
	s_mov_b32 m0, s71
	s_mov_b64 s[26:27], 0xe0080
	global_load_lds_dwordx4 v5, s[24:25]
	v_lshl_add_u64 v[6:7], v[2:3], 0, s[26:27]
	v_mov_b32_e32 v5, v203
	s_add_i32 m0, s60, 0x1c000
	v_readfirstlane_b32 s6, v6
	v_readfirstlane_b32 s7, v7
	v_lshlrev_b32_e32 v6, 1, v4
	v_lshlrev_b32_e32 v7, 2, v0
	v_lshlrev_b32_e32 v8, 6, v0
	v_and_b32_e32 v7, 32, v7
	v_or_b32_e32 v212, s3, v4
	global_load_lds_dwordx4 v5, s[6:7]
	v_mov_b32_e32 v5, v205
	s_add_i32 m0, s60, 0x1e000
	s_cmpk_lt_u32 s4, 0x100
	global_load_lds_dwordx4 v5, s[6:7]
	v_and_b32_e32 v5, 15, v0
	v_lshl_or_b32 v210, s2, 6, v5
	s_movk_i32 s2, 0x3c0
	v_lshl_or_b32 v5, v5, 6, v6
	v_and_or_b32 v6, v8, s2, v6
	v_bitop3_b32 v211, s28, v6, v7 bitop3:0xf6
	s_waitcnt vmcnt(6)
	v_bitop3_b32 v5, v5, s5, v7 bitop3:0xde
	s_cselect_b64 s[28:29], -1, 0
	s_add_i32 s2, 0, 0x20160
	v_add_u32_e32 v4, 0, v211
	v_mov_b32_e32 v213, s2
	s_add_i32 s72, 0, 0x20144
	s_add_i32 s73, 0, 0x20148
	s_add_i32 s74, 0, 0x2014c
	s_add_i32 s75, 0, 0x20150
	s_add_i32 s76, 0, 0x20154
	s_add_i32 s77, 0, 0x20158
	s_add_i32 s78, 0, 0x2015c
	s_mov_b64 s[30:31], 0x100
	v_add_u32_e32 v214, 0x10000, v4
	v_add_u32_e32 v215, 0x14000, v4
	v_add_u32_e32 v216, 0, v5
	s_add_i32 s79, s60, 0xc000
	s_add_i32 s80, s60, 0xe000
	v_mov_b32_e32 v217, 0x7f
	s_mov_b32 s34, 0x3b000000
	s_mov_b64 s[40:41], 0x10000
	s_mov_b64 s[42:43], 0x20000
	s_mov_b32 s81, 0x20000
	s_mov_b64 s[44:45], 0x30000
	s_mov_b32 s82, 0x30000
	s_mov_b64 s[46:47], 0x80000
	s_mov_b32 s83, 0x80000
	s_mov_b64 s[48:49], 0x90000
	s_mov_b32 s84, 0x90000
	s_mov_b64 s[50:51], 0xa0000
	s_mov_b32 s85, 0xa0000
	s_mov_b64 s[52:53], 0xb0000
	s_mov_b32 s86, 0xb0000
	s_barrier
	s_branch .LBB0_2629
	s_nop 0
